# conv tap loop head: first seven LDS row pairs read straight into their destination registers with 14 reads in flight instead of one serialized round trip per pair
# baseline (speedup 1.0000x reference)
.LBB0_546:
	s_mul_i32 s5, s30, 0x2080
	s_mul_i32 s4, s31, 0x2080
	v_add_u32_e32 v223, s5, v222
	v_add_u32_e32 v232, s4, v222
	ds_read_u16 v194, v223
	ds_read_u16 v195, v232
	ds_read_u16 v196, v223 offset:1040
	ds_read_u16 v197, v232 offset:1040
	ds_read_u16 v224, v223 offset:2080
	ds_read_u16 v225, v232 offset:2080
	ds_read_u16 v226, v223 offset:3120
	ds_read_u16 v227, v232 offset:3120
	ds_read_u16 v218, v223 offset:4160
	ds_read_u16 v219, v232 offset:4160
	ds_read_u16 v198, v223 offset:5200
	ds_read_u16 v199, v232 offset:5200
	ds_read_u16 v174, v223 offset:6240
	ds_read_u16 v175, v232 offset:6240
	s_add_i32 s30, s30, 2
	s_add_i32 s31, s31, 2
	s_add_i32 s33, s33, -2
	s_cmp_lg_u32 s33, 0
	s_waitcnt lgkmcnt(12)
	v_lshlrev_b32_e32 v194, 16, v194
	v_lshlrev_b32_e32 v195, 16, v195
	ds_read_u16 v154, v223 offset:7280
	ds_read_u16 v155, v232 offset:7280
	v_pk_fma_f32 v[194:195], v[42:43], v[194:195], v[152:153]
	s_waitcnt lgkmcnt(12)
	v_lshlrev_b32_e32 v196, 16, v196
	v_lshlrev_b32_e32 v197, 16, v197
	ds_read_u16 v156, v223 offset:8320
	ds_read_u16 v157, v232 offset:8320
	v_pk_fma_f32 v[194:195], v[44:45], v[196:197], v[194:195]
	v_pk_fma_f32 v[196:197], v[42:43], v[196:197], v[152:153]
	s_waitcnt lgkmcnt(12)
	v_lshlrev_b32_e32 v224, 16, v224
	v_lshlrev_b32_e32 v225, 16, v225
	ds_read_u16 v158, v223 offset:9360
	ds_read_u16 v159, v232 offset:9360
	v_pk_fma_f32 v[194:195], v[46:47], v[224:225], v[194:195]
	v_pk_fma_f32 v[196:197], v[44:45], v[224:225], v[196:197]
	v_pk_fma_f32 v[224:225], v[42:43], v[224:225], v[152:153]
	s_waitcnt lgkmcnt(12)
	v_lshlrev_b32_e32 v226, 16, v226
	v_lshlrev_b32_e32 v227, 16, v227
	ds_read_u16 v160, v223 offset:10400
	ds_read_u16 v161, v232 offset:10400
	v_pk_fma_f32 v[194:195], v[48:49], v[226:227], v[194:195]
	v_pk_fma_f32 v[196:197], v[46:47], v[226:227], v[196:197]
	v_pk_fma_f32 v[224:225], v[44:45], v[226:227], v[224:225]
	s_waitcnt lgkmcnt(12)
	v_lshlrev_b32_e32 v218, 16, v218
	v_lshlrev_b32_e32 v219, 16, v219
	ds_read_u16 v162, v223 offset:11440
	ds_read_u16 v163, v232 offset:11440
	v_pk_fma_f32 v[226:227], v[42:43], v[226:227], v[152:153]
	v_pk_fma_f32 v[194:195], v[50:51], v[218:219], v[194:195]
	v_pk_fma_f32 v[196:197], v[48:49], v[218:219], v[196:197]
	s_waitcnt lgkmcnt(12)
	v_lshlrev_b32_e32 v198, 16, v198
	v_lshlrev_b32_e32 v199, 16, v199
	v_pk_fma_f32 v[224:225], v[46:47], v[218:219], v[224:225]
	v_pk_fma_f32 v[226:227], v[44:45], v[218:219], v[226:227]
	v_pk_fma_f32 v[218:219], v[42:43], v[218:219], v[152:153]
	s_waitcnt lgkmcnt(10)
	v_lshlrev_b32_e32 v174, 16, v174
	v_lshlrev_b32_e32 v175, 16, v175
	v_pk_fma_f32 v[194:195], v[52:53], v[198:199], v[194:195]
	v_pk_fma_f32 v[196:197], v[50:51], v[198:199], v[196:197]
	v_pk_fma_f32 v[224:225], v[48:49], v[198:199], v[224:225]
	v_pk_fma_f32 v[226:227], v[46:47], v[198:199], v[226:227]
	v_pk_fma_f32 v[218:219], v[44:45], v[198:199], v[218:219]
	v_pk_fma_f32 v[198:199], v[42:43], v[198:199], v[152:153]
	s_waitcnt lgkmcnt(8)
	v_lshlrev_b32_e32 v155, 16, v155
	v_lshlrev_b32_e32 v154, 16, v154
	ds_read_u16 v164, v223 offset:12480
	ds_read_u16 v165, v232 offset:12480
	v_pk_fma_f32 v[194:195], v[54:55], v[174:175], v[194:195]
	v_pk_fma_f32 v[196:197], v[52:53], v[174:175], v[196:197]
	v_pk_fma_f32 v[224:225], v[50:51], v[174:175], v[224:225]
	v_pk_fma_f32 v[226:227], v[48:49], v[174:175], v[226:227]
	v_pk_fma_f32 v[218:219], v[46:47], v[174:175], v[218:219]
	v_pk_fma_f32 v[198:199], v[44:45], v[174:175], v[198:199]
	v_pk_fma_f32 v[174:175], v[42:43], v[174:175], v[152:153]
	s_waitcnt lgkmcnt(8)
	v_lshlrev_b32_e32 v157, 16, v157
	v_lshlrev_b32_e32 v156, 16, v156
	ds_read_u16 v166, v223 offset:13520
	ds_read_u16 v167, v232 offset:13520
	v_pk_fma_f32 v[194:195], v[56:57], v[154:155], v[194:195]
	v_pk_fma_f32 v[196:197], v[54:55], v[154:155], v[196:197]
	v_pk_fma_f32 v[224:225], v[52:53], v[154:155], v[224:225]
	v_pk_fma_f32 v[226:227], v[50:51], v[154:155], v[226:227]
	v_pk_fma_f32 v[218:219], v[48:49], v[154:155], v[218:219]
	v_pk_fma_f32 v[198:199], v[46:47], v[154:155], v[198:199]
	v_pk_fma_f32 v[174:175], v[44:45], v[154:155], v[174:175]
	v_pk_fma_f32 v[154:155], v[42:43], v[154:155], v[152:153]
	s_waitcnt lgkmcnt(8)
	v_lshlrev_b32_e32 v159, 16, v159
	v_lshlrev_b32_e32 v158, 16, v158
	ds_read_u16 v168, v223 offset:14560
	ds_read_u16 v169, v232 offset:14560
	v_pk_fma_f32 v[154:155], v[44:45], v[156:157], v[154:155]
	s_waitcnt lgkmcnt(8)
	v_lshlrev_b32_e32 v161, 16, v161
	v_lshlrev_b32_e32 v160, 16, v160
	ds_read_u16 v170, v223 offset:15600
	ds_read_u16 v171, v232 offset:15600
	v_pk_fma_f32 v[194:195], v[58:59], v[156:157], v[194:195]
	v_pk_fma_f32 v[196:197], v[56:57], v[156:157], v[196:197]
	v_pk_fma_f32 v[224:225], v[54:55], v[156:157], v[224:225]
	v_pk_fma_f32 v[226:227], v[52:53], v[156:157], v[226:227]
	v_pk_fma_f32 v[218:219], v[50:51], v[156:157], v[218:219]
	v_pk_fma_f32 v[198:199], v[48:49], v[156:157], v[198:199]
	v_pk_fma_f32 v[174:175], v[46:47], v[156:157], v[174:175]
	v_pk_fma_f32 v[154:155], v[46:47], v[158:159], v[154:155]
	s_waitcnt lgkmcnt(8)
	v_lshlrev_b32_e32 v163, 16, v163
	v_lshlrev_b32_e32 v162, 16, v162
	ds_read_u16 v172, v223 offset:16640
	ds_read_u16 v173, v232 offset:16640
	v_pk_fma_f32 v[194:195], v[60:61], v[158:159], v[194:195]
	v_pk_fma_f32 v[196:197], v[58:59], v[158:159], v[196:197]
	v_pk_fma_f32 v[224:225], v[56:57], v[158:159], v[224:225]
	v_pk_fma_f32 v[226:227], v[54:55], v[158:159], v[226:227]
	v_pk_fma_f32 v[218:219], v[52:53], v[158:159], v[218:219]
	v_pk_fma_f32 v[198:199], v[50:51], v[158:159], v[198:199]
	v_pk_fma_f32 v[174:175], v[48:49], v[158:159], v[174:175]
	v_pk_fma_f32 v[154:155], v[48:49], v[160:161], v[154:155]
	s_waitcnt lgkmcnt(8)
	v_lshlrev_b32_e32 v165, 16, v165
	v_lshlrev_b32_e32 v164, 16, v164
	ds_read_u16 v176, v223 offset:17680
	ds_read_u16 v177, v232 offset:17680
	v_pk_fma_f32 v[194:195], v[62:63], v[160:161], v[194:195]
	v_pk_fma_f32 v[196:197], v[60:61], v[160:161], v[196:197]
	v_pk_fma_f32 v[224:225], v[58:59], v[160:161], v[224:225]
	v_pk_fma_f32 v[226:227], v[56:57], v[160:161], v[226:227]
	v_pk_fma_f32 v[218:219], v[54:55], v[160:161], v[218:219]
	v_pk_fma_f32 v[198:199], v[52:53], v[160:161], v[198:199]
	v_pk_fma_f32 v[174:175], v[50:51], v[160:161], v[174:175]
	v_pk_fma_f32 v[154:155], v[50:51], v[162:163], v[154:155]
	s_waitcnt lgkmcnt(8)
	v_lshlrev_b32_e32 v167, 16, v167
	v_lshlrev_b32_e32 v166, 16, v166
	ds_read_u16 v178, v223 offset:18720
	ds_read_u16 v179, v232 offset:18720
	v_pk_fma_f32 v[194:195], v[64:65], v[162:163], v[194:195]
	v_pk_fma_f32 v[196:197], v[62:63], v[162:163], v[196:197]
	v_pk_fma_f32 v[224:225], v[60:61], v[162:163], v[224:225]
	v_pk_fma_f32 v[226:227], v[58:59], v[162:163], v[226:227]
	v_pk_fma_f32 v[218:219], v[56:57], v[162:163], v[218:219]
	v_pk_fma_f32 v[198:199], v[54:55], v[162:163], v[198:199]
	v_pk_fma_f32 v[174:175], v[52:53], v[162:163], v[174:175]
	v_pk_fma_f32 v[154:155], v[52:53], v[164:165], v[154:155]
	s_waitcnt lgkmcnt(8)
	v_lshlrev_b32_e32 v169, 16, v169
	v_lshlrev_b32_e32 v168, 16, v168
	ds_read_u16 v180, v223 offset:19760
	ds_read_u16 v181, v232 offset:19760
	v_pk_fma_f32 v[194:195], v[114:115], v[164:165], v[194:195]
	v_pk_fma_f32 v[196:197], v[64:65], v[164:165], v[196:197]
	v_pk_fma_f32 v[224:225], v[62:63], v[164:165], v[224:225]
	v_pk_fma_f32 v[226:227], v[60:61], v[164:165], v[226:227]
	v_pk_fma_f32 v[218:219], v[58:59], v[164:165], v[218:219]
	v_pk_fma_f32 v[198:199], v[56:57], v[164:165], v[198:199]
	v_pk_fma_f32 v[174:175], v[54:55], v[164:165], v[174:175]
	v_pk_fma_f32 v[154:155], v[54:55], v[166:167], v[154:155]
	s_waitcnt lgkmcnt(8)
	v_lshlrev_b32_e32 v171, 16, v171
	v_lshlrev_b32_e32 v170, 16, v170
	ds_read_u16 v182, v223 offset:20800
	ds_read_u16 v183, v232 offset:20800
	v_pk_fma_f32 v[194:195], v[116:117], v[166:167], v[194:195]
	v_pk_fma_f32 v[196:197], v[114:115], v[166:167], v[196:197]
	v_pk_fma_f32 v[224:225], v[64:65], v[166:167], v[224:225]
	v_pk_fma_f32 v[226:227], v[62:63], v[166:167], v[226:227]
	v_pk_fma_f32 v[218:219], v[60:61], v[166:167], v[218:219]
	v_pk_fma_f32 v[198:199], v[58:59], v[166:167], v[198:199]
	v_pk_fma_f32 v[174:175], v[56:57], v[166:167], v[174:175]
	v_pk_fma_f32 v[154:155], v[56:57], v[168:169], v[154:155]
	s_waitcnt lgkmcnt(8)
	v_lshlrev_b32_e32 v173, 16, v173
	v_lshlrev_b32_e32 v172, 16, v172
	ds_read_u16 v184, v223 offset:21840
	ds_read_u16 v185, v232 offset:21840
	v_pk_fma_f32 v[194:195], v[118:119], v[168:169], v[194:195]
	v_pk_fma_f32 v[196:197], v[116:117], v[168:169], v[196:197]
	v_pk_fma_f32 v[224:225], v[114:115], v[168:169], v[224:225]
	v_pk_fma_f32 v[226:227], v[64:65], v[168:169], v[226:227]
	v_pk_fma_f32 v[218:219], v[62:63], v[168:169], v[218:219]
	v_pk_fma_f32 v[198:199], v[60:61], v[168:169], v[198:199]
	v_pk_fma_f32 v[174:175], v[58:59], v[168:169], v[174:175]
	v_pk_fma_f32 v[154:155], v[58:59], v[170:171], v[154:155]
	s_waitcnt lgkmcnt(8)
	v_lshlrev_b32_e32 v177, 16, v177
	v_lshlrev_b32_e32 v176, 16, v176
	ds_read_u16 v186, v223 offset:22880
	ds_read_u16 v187, v232 offset:22880
	v_pk_fma_f32 v[194:195], v[120:121], v[170:171], v[194:195]
	v_pk_fma_f32 v[196:197], v[118:119], v[170:171], v[196:197]
	v_pk_fma_f32 v[224:225], v[116:117], v[170:171], v[224:225]
	v_pk_fma_f32 v[226:227], v[114:115], v[170:171], v[226:227]
	v_pk_fma_f32 v[218:219], v[64:65], v[170:171], v[218:219]
	v_pk_fma_f32 v[198:199], v[62:63], v[170:171], v[198:199]
	v_pk_fma_f32 v[174:175], v[60:61], v[170:171], v[174:175]
	v_pk_fma_f32 v[154:155], v[60:61], v[172:173], v[154:155]
	s_waitcnt lgkmcnt(8)
	v_lshlrev_b32_e32 v179, 16, v179
	v_lshlrev_b32_e32 v178, 16, v178
	ds_read_u16 v188, v223 offset:23920
	ds_read_u16 v189, v232 offset:23920
	v_pk_fma_f32 v[194:195], v[122:123], v[172:173], v[194:195]
	v_pk_fma_f32 v[196:197], v[120:121], v[172:173], v[196:197]
	v_pk_fma_f32 v[224:225], v[118:119], v[172:173], v[224:225]
	v_pk_fma_f32 v[226:227], v[116:117], v[172:173], v[226:227]
	v_pk_fma_f32 v[218:219], v[114:115], v[172:173], v[218:219]
	v_pk_fma_f32 v[198:199], v[64:65], v[172:173], v[198:199]
	v_pk_fma_f32 v[174:175], v[62:63], v[172:173], v[174:175]
	v_pk_fma_f32 v[154:155], v[62:63], v[176:177], v[154:155]
	s_waitcnt lgkmcnt(8)
	v_lshlrev_b32_e32 v181, 16, v181
	v_lshlrev_b32_e32 v180, 16, v180
	ds_read_u16 v190, v223 offset:24960
	ds_read_u16 v191, v232 offset:24960
	v_pk_fma_f32 v[194:195], v[124:125], v[176:177], v[194:195]
	v_pk_fma_f32 v[196:197], v[122:123], v[176:177], v[196:197]
	v_pk_fma_f32 v[224:225], v[120:121], v[176:177], v[224:225]
	v_pk_fma_f32 v[226:227], v[118:119], v[176:177], v[226:227]
	v_pk_fma_f32 v[218:219], v[116:117], v[176:177], v[218:219]
	v_pk_fma_f32 v[198:199], v[114:115], v[176:177], v[198:199]
	v_pk_fma_f32 v[174:175], v[64:65], v[176:177], v[174:175]
	v_pk_fma_f32 v[154:155], v[64:65], v[178:179], v[154:155]
	s_waitcnt lgkmcnt(8)
	v_lshlrev_b32_e32 v183, 16, v183
	v_lshlrev_b32_e32 v182, 16, v182
	ds_read_u16 v192, v223 offset:26000
	ds_read_u16 v193, v232 offset:26000
	v_pk_fma_f32 v[194:195], v[126:127], v[178:179], v[194:195]
	v_pk_fma_f32 v[196:197], v[124:125], v[178:179], v[196:197]
	v_pk_fma_f32 v[224:225], v[122:123], v[178:179], v[224:225]
	v_pk_fma_f32 v[226:227], v[120:121], v[178:179], v[226:227]
	v_pk_fma_f32 v[218:219], v[118:119], v[178:179], v[218:219]
	v_pk_fma_f32 v[198:199], v[116:117], v[178:179], v[198:199]
	v_pk_fma_f32 v[174:175], v[114:115], v[178:179], v[174:175]
	v_pk_fma_f32 v[154:155], v[114:115], v[180:181], v[154:155]
	s_waitcnt lgkmcnt(8)
	v_lshlrev_b32_e32 v185, 16, v185
	v_lshlrev_b32_e32 v184, 16, v184
	ds_read_u16 v200, v223 offset:27040
	ds_read_u16 v201, v232 offset:27040
	v_pk_fma_f32 v[194:195], v[128:129], v[180:181], v[194:195]
	v_pk_fma_f32 v[196:197], v[126:127], v[180:181], v[196:197]
	v_pk_fma_f32 v[224:225], v[124:125], v[180:181], v[224:225]
	v_pk_fma_f32 v[226:227], v[122:123], v[180:181], v[226:227]
	v_pk_fma_f32 v[218:219], v[120:121], v[180:181], v[218:219]
	v_pk_fma_f32 v[198:199], v[118:119], v[180:181], v[198:199]
	v_pk_fma_f32 v[174:175], v[116:117], v[180:181], v[174:175]
	v_pk_fma_f32 v[154:155], v[116:117], v[182:183], v[154:155]
	s_waitcnt lgkmcnt(8)
	v_lshlrev_b32_e32 v187, 16, v187
	v_lshlrev_b32_e32 v186, 16, v186
	ds_read_u16 v202, v223 offset:28080
	ds_read_u16 v203, v232 offset:28080
	v_pk_fma_f32 v[194:195], v[130:131], v[182:183], v[194:195]
	v_pk_fma_f32 v[196:197], v[128:129], v[182:183], v[196:197]
	v_pk_fma_f32 v[224:225], v[126:127], v[182:183], v[224:225]
	v_pk_fma_f32 v[226:227], v[124:125], v[182:183], v[226:227]
	v_pk_fma_f32 v[218:219], v[122:123], v[182:183], v[218:219]
	v_pk_fma_f32 v[198:199], v[120:121], v[182:183], v[198:199]
	v_pk_fma_f32 v[174:175], v[118:119], v[182:183], v[174:175]
	v_pk_fma_f32 v[154:155], v[118:119], v[184:185], v[154:155]
	s_waitcnt lgkmcnt(8)
	v_lshlrev_b32_e32 v189, 16, v189
	v_lshlrev_b32_e32 v188, 16, v188
	ds_read_u16 v204, v223 offset:29120
	ds_read_u16 v205, v232 offset:29120
	v_pk_fma_f32 v[194:195], v[132:133], v[184:185], v[194:195]
	v_pk_fma_f32 v[196:197], v[130:131], v[184:185], v[196:197]
	v_pk_fma_f32 v[224:225], v[128:129], v[184:185], v[224:225]
	v_pk_fma_f32 v[226:227], v[126:127], v[184:185], v[226:227]
	v_pk_fma_f32 v[218:219], v[124:125], v[184:185], v[218:219]
	v_pk_fma_f32 v[198:199], v[122:123], v[184:185], v[198:199]
	v_pk_fma_f32 v[174:175], v[120:121], v[184:185], v[174:175]
	v_pk_fma_f32 v[154:155], v[120:121], v[186:187], v[154:155]
	s_waitcnt lgkmcnt(8)
	v_lshlrev_b32_e32 v191, 16, v191
	v_lshlrev_b32_e32 v190, 16, v190
	ds_read_u16 v206, v223 offset:30160
	ds_read_u16 v207, v232 offset:30160
	v_pk_fma_f32 v[194:195], v[134:135], v[186:187], v[194:195]
	v_pk_fma_f32 v[196:197], v[132:133], v[186:187], v[196:197]
	v_pk_fma_f32 v[224:225], v[130:131], v[186:187], v[224:225]
	v_pk_fma_f32 v[226:227], v[128:129], v[186:187], v[226:227]
	v_pk_fma_f32 v[218:219], v[126:127], v[186:187], v[218:219]
	v_pk_fma_f32 v[198:199], v[124:125], v[186:187], v[198:199]
	v_pk_fma_f32 v[174:175], v[122:123], v[186:187], v[174:175]
	v_pk_fma_f32 v[154:155], v[122:123], v[188:189], v[154:155]
	s_waitcnt lgkmcnt(8)
	v_lshlrev_b32_e32 v193, 16, v193
	v_lshlrev_b32_e32 v192, 16, v192
	ds_read_u16 v208, v223 offset:31200
	ds_read_u16 v209, v232 offset:31200
	v_pk_fma_f32 v[194:195], v[136:137], v[188:189], v[194:195]
	v_pk_fma_f32 v[196:197], v[134:135], v[188:189], v[196:197]
	v_pk_fma_f32 v[224:225], v[132:133], v[188:189], v[224:225]
	v_pk_fma_f32 v[226:227], v[130:131], v[188:189], v[226:227]
	v_pk_fma_f32 v[218:219], v[128:129], v[188:189], v[218:219]
	v_pk_fma_f32 v[198:199], v[126:127], v[188:189], v[198:199]
	v_pk_fma_f32 v[174:175], v[124:125], v[188:189], v[174:175]
	v_pk_fma_f32 v[154:155], v[124:125], v[190:191], v[154:155]
	s_waitcnt lgkmcnt(8)
	v_lshlrev_b32_e32 v201, 16, v201
	v_lshlrev_b32_e32 v200, 16, v200
	ds_read_u16 v210, v223 offset:32240
	ds_read_u16 v211, v232 offset:32240
	v_pk_fma_f32 v[194:195], v[138:139], v[190:191], v[194:195]
	v_pk_fma_f32 v[196:197], v[136:137], v[190:191], v[196:197]
	v_pk_fma_f32 v[224:225], v[134:135], v[190:191], v[224:225]
	v_pk_fma_f32 v[226:227], v[132:133], v[190:191], v[226:227]
	v_pk_fma_f32 v[218:219], v[130:131], v[190:191], v[218:219]
	v_pk_fma_f32 v[198:199], v[128:129], v[190:191], v[198:199]
	v_pk_fma_f32 v[174:175], v[126:127], v[190:191], v[174:175]
	v_pk_fma_f32 v[154:155], v[126:127], v[192:193], v[154:155]
	s_waitcnt lgkmcnt(8)
	v_lshlrev_b32_e32 v203, 16, v203
	v_lshlrev_b32_e32 v202, 16, v202
	ds_read_u16 v212, v223 offset:33280
	ds_read_u16 v213, v232 offset:33280
	v_pk_fma_f32 v[194:195], v[140:141], v[192:193], v[194:195]
	v_pk_fma_f32 v[196:197], v[138:139], v[192:193], v[196:197]
	v_pk_fma_f32 v[224:225], v[136:137], v[192:193], v[224:225]
	v_pk_fma_f32 v[226:227], v[134:135], v[192:193], v[226:227]
	v_pk_fma_f32 v[218:219], v[132:133], v[192:193], v[218:219]
	v_pk_fma_f32 v[198:199], v[130:131], v[192:193], v[198:199]
	v_pk_fma_f32 v[174:175], v[128:129], v[192:193], v[174:175]
	v_pk_fma_f32 v[154:155], v[128:129], v[200:201], v[154:155]
	s_waitcnt lgkmcnt(8)
	v_lshlrev_b32_e32 v205, 16, v205
	v_lshlrev_b32_e32 v204, 16, v204
	ds_read_u16 v214, v223 offset:34320
	ds_read_u16 v215, v232 offset:34320
	v_pk_fma_f32 v[194:195], v[142:143], v[200:201], v[194:195]
	v_pk_fma_f32 v[196:197], v[140:141], v[200:201], v[196:197]
	v_pk_fma_f32 v[224:225], v[138:139], v[200:201], v[224:225]
	v_pk_fma_f32 v[226:227], v[136:137], v[200:201], v[226:227]
	v_pk_fma_f32 v[218:219], v[134:135], v[200:201], v[218:219]
	v_pk_fma_f32 v[198:199], v[132:133], v[200:201], v[198:199]
	v_pk_fma_f32 v[174:175], v[130:131], v[200:201], v[174:175]
	v_pk_fma_f32 v[154:155], v[130:131], v[202:203], v[154:155]
	s_waitcnt lgkmcnt(8)
	v_lshlrev_b32_e32 v207, 16, v207
	v_lshlrev_b32_e32 v206, 16, v206
	ds_read_u16 v216, v223 offset:35360
	ds_read_u16 v217, v232 offset:35360
	v_pk_fma_f32 v[194:195], v[144:145], v[202:203], v[194:195]
	v_pk_fma_f32 v[196:197], v[142:143], v[202:203], v[196:197]
	v_pk_fma_f32 v[224:225], v[140:141], v[202:203], v[224:225]
	v_pk_fma_f32 v[226:227], v[138:139], v[202:203], v[226:227]
	v_pk_fma_f32 v[218:219], v[136:137], v[202:203], v[218:219]
	v_pk_fma_f32 v[198:199], v[134:135], v[202:203], v[198:199]
	v_pk_fma_f32 v[174:175], v[132:133], v[202:203], v[174:175]
	v_pk_fma_f32 v[154:155], v[132:133], v[204:205], v[154:155]
	s_waitcnt lgkmcnt(8)
	v_lshlrev_b32_e32 v209, 16, v209
	v_lshlrev_b32_e32 v208, 16, v208
	ds_read_u16 v220, v223 offset:36400
	ds_read_u16 v221, v232 offset:36400
	v_pk_fma_f32 v[194:195], v[146:147], v[204:205], v[194:195]
	v_pk_fma_f32 v[196:197], v[144:145], v[204:205], v[196:197]
	v_pk_fma_f32 v[224:225], v[142:143], v[204:205], v[224:225]
	v_pk_fma_f32 v[226:227], v[140:141], v[204:205], v[226:227]
	v_pk_fma_f32 v[218:219], v[138:139], v[204:205], v[218:219]
	v_pk_fma_f32 v[198:199], v[136:137], v[204:205], v[198:199]
	v_pk_fma_f32 v[174:175], v[134:135], v[204:205], v[174:175]
	v_pk_fma_f32 v[154:155], v[134:135], v[206:207], v[154:155]
	s_waitcnt lgkmcnt(8)
	v_lshlrev_b32_e32 v211, 16, v211
	v_lshlrev_b32_e32 v210, 16, v210
	ds_read_u16 v228, v223 offset:37440
	ds_read_u16 v229, v232 offset:37440
	v_pk_fma_f32 v[194:195], v[148:149], v[206:207], v[194:195]
	v_pk_fma_f32 v[196:197], v[146:147], v[206:207], v[196:197]
	v_pk_fma_f32 v[224:225], v[144:145], v[206:207], v[224:225]
	v_pk_fma_f32 v[226:227], v[142:143], v[206:207], v[226:227]
	v_pk_fma_f32 v[218:219], v[140:141], v[206:207], v[218:219]
	v_pk_fma_f32 v[198:199], v[138:139], v[206:207], v[198:199]
	v_pk_fma_f32 v[174:175], v[136:137], v[206:207], v[174:175]
	v_pk_fma_f32 v[154:155], v[136:137], v[208:209], v[154:155]
	s_waitcnt lgkmcnt(8)
	v_lshlrev_b32_e32 v213, 16, v213
	v_lshlrev_b32_e32 v212, 16, v212
	ds_read_u16 v230, v223 offset:38480
	ds_read_u16 v231, v232 offset:38480
	v_pk_fma_f32 v[194:195], v[150:151], v[208:209], v[194:195]
	v_pk_fma_f32 v[196:197], v[148:149], v[208:209], v[196:197]
	v_pk_fma_f32 v[224:225], v[146:147], v[208:209], v[224:225]
	v_pk_fma_f32 v[226:227], v[144:145], v[208:209], v[226:227]
	v_pk_fma_f32 v[218:219], v[142:143], v[208:209], v[218:219]
	v_pk_fma_f32 v[198:199], v[140:141], v[208:209], v[198:199]
	v_pk_fma_f32 v[174:175], v[138:139], v[208:209], v[174:175]
	v_pk_fma_f32 v[154:155], v[138:139], v[210:211], v[154:155]
	s_waitcnt lgkmcnt(8)
	v_lshlrev_b32_e32 v215, 16, v215
	v_lshlrev_b32_e32 v214, 16, v214
	v_pk_fma_f32 v[196:197], v[150:151], v[210:211], v[196:197]
	v_pk_fma_f32 v[224:225], v[148:149], v[210:211], v[224:225]
	v_pk_fma_f32 v[226:227], v[146:147], v[210:211], v[226:227]
	v_pk_fma_f32 v[218:219], v[144:145], v[210:211], v[218:219]
	v_pk_fma_f32 v[198:199], v[142:143], v[210:211], v[198:199]
	v_pk_fma_f32 v[174:175], v[140:141], v[210:211], v[174:175]
	v_pk_fma_f32 v[154:155], v[140:141], v[212:213], v[154:155]
	v_cvt_pk_bf16_f32 v156, v194, v195
	s_waitcnt lgkmcnt(6)
	v_lshlrev_b32_e32 v217, 16, v217
	v_lshlrev_b32_e32 v216, 16, v216
	v_pk_fma_f32 v[224:225], v[150:151], v[212:213], v[224:225]
	v_pk_fma_f32 v[226:227], v[148:149], v[212:213], v[226:227]
	v_pk_fma_f32 v[218:219], v[146:147], v[212:213], v[218:219]
	v_pk_fma_f32 v[198:199], v[144:145], v[212:213], v[198:199]
	v_pk_fma_f32 v[174:175], v[142:143], v[212:213], v[174:175]
	v_pk_fma_f32 v[154:155], v[142:143], v[214:215], v[154:155]
	ds_write_b16 v223, v156
	ds_write_b16_d16_hi v232, v156
	v_cvt_pk_bf16_f32 v156, v196, v197
	s_waitcnt lgkmcnt(6)
	v_lshlrev_b32_e32 v221, 16, v221
	v_lshlrev_b32_e32 v220, 16, v220
	v_pk_fma_f32 v[226:227], v[150:151], v[214:215], v[226:227]
	v_pk_fma_f32 v[218:219], v[148:149], v[214:215], v[218:219]
	v_pk_fma_f32 v[198:199], v[146:147], v[214:215], v[198:199]
	v_pk_fma_f32 v[174:175], v[144:145], v[214:215], v[174:175]
	v_pk_fma_f32 v[154:155], v[144:145], v[216:217], v[154:155]
	ds_write_b16 v223, v156 offset:1040
	ds_write_b16_d16_hi v232, v156 offset:1040
	v_cvt_pk_bf16_f32 v156, v224, v225
	s_waitcnt lgkmcnt(6)
	v_lshlrev_b32_e32 v229, 16, v229
	v_lshlrev_b32_e32 v228, 16, v228
	v_pk_fma_f32 v[218:219], v[150:151], v[216:217], v[218:219]
	v_pk_fma_f32 v[198:199], v[148:149], v[216:217], v[198:199]
	v_pk_fma_f32 v[174:175], v[146:147], v[216:217], v[174:175]
	v_pk_fma_f32 v[154:155], v[146:147], v[220:221], v[154:155]
	ds_write_b16 v223, v156 offset:2080
	ds_write_b16_d16_hi v232, v156 offset:2080
	v_cvt_pk_bf16_f32 v156, v226, v227
	s_waitcnt lgkmcnt(6)
	v_lshlrev_b32_e32 v231, 16, v231
	v_lshlrev_b32_e32 v230, 16, v230
	v_pk_fma_f32 v[198:199], v[150:151], v[220:221], v[198:199]
	v_pk_fma_f32 v[174:175], v[148:149], v[220:221], v[174:175]
	v_pk_fma_f32 v[154:155], v[148:149], v[228:229], v[154:155]
	ds_write_b16 v223, v156 offset:3120
	ds_write_b16_d16_hi v232, v156 offset:3120
	v_cvt_pk_bf16_f32 v156, v218, v219
	v_pk_fma_f32 v[174:175], v[150:151], v[228:229], v[174:175]
	v_pk_fma_f32 v[154:155], v[150:151], v[230:231], v[154:155]
	ds_write_b16 v223, v156 offset:4160
	ds_write_b16_d16_hi v232, v156 offset:4160
	v_cvt_pk_bf16_f32 v156, v198, v199
	ds_write_b16 v223, v156 offset:5200
	ds_write_b16_d16_hi v232, v156 offset:5200
	v_cvt_pk_bf16_f32 v156, v174, v175
	v_cvt_pk_bf16_f32 v154, v154, v155
	ds_write_b16 v223, v156 offset:6240
	ds_write_b16_d16_hi v232, v156 offset:6240
	ds_write_b16 v223, v154 offset:7280
	ds_write_b16_d16_hi v232, v154 offset:7280
	s_cbranch_scc1 .LBB0_546
	s_lshl_b64 s[38:39], s[52:53], 2
	s_add_u32 s4, s26, s38
	v_and_b32_e32 v52, 63, v0
	s_addc_u32 s5, s27, s39
	v_ashrrev_i32_e32 v50, 6, v0
	v_lshlrev_b32_e32 v0, 5, v52
	s_waitcnt lgkmcnt(0)
	s_barrier
	global_load_dwordx4 v[42:45], v0, s[4:5] offset:16
	global_load_dwordx4 v[46:49], v0, s[4:5]
	v_lshlrev_b32_e32 v0, 4, v52
	v_mul_lo_u32 v51, v50, s44
	v_add3_u32 v0, 0, v0, v51
	ds_read_b128 v[60:63], v0
	ds_read_b128 v[138:141], v0 offset:24960
	ds_read_b128 v[142:145], v0 offset:33280
	ds_read_b128 v[170:173], v0 offset:58240
	ds_read_b128 v[118:121], v0 offset:8320
	s_add_u32 s30, s28, 0x27c40000
	s_waitcnt lgkmcnt(3)
	v_lshlrev_b32_e32 v132, 16, v138
	v_and_b32_e32 v130, 0xffff0000, v138
	v_lshlrev_b32_e32 v134, 16, v139
	v_and_b32_e32 v133, 0xffff0000, v139
	v_lshlrev_b32_e32 v136, 16, v140
	v_and_b32_e32 v135, 0xffff0000, v140
	v_lshlrev_b32_e32 v139, 16, v141
	v_and_b32_e32 v137, 0xffff0000, v141
	s_waitcnt lgkmcnt(2)
	v_lshlrev_b32_e32 v141, 16, v142
	v_and_b32_e32 v138, 0xffff0000, v142
	v_lshlrev_b32_e32 v142, 16, v143
	v_and_b32_e32 v140, 0xffff0000, v143
	v_lshlrev_b32_e32 v150, 16, v144
	v_and_b32_e32 v143, 0xffff0000, v144
	v_lshlrev_b32_e32 v161, 16, v145
	v_and_b32_e32 v151, 0xffff0000, v145
	ds_read_b128 v[144:147], v0 offset:41600
	v_and_b32_e32 v53, 0xffff0000, v60
	v_and_b32_e32 v54, 0xffff0000, v61
	v_lshlrev_b32_e32 v55, 16, v60
	v_mul_f32_e32 v51, v53, v53
	v_lshlrev_b32_e32 v56, 16, v61
	v_mul_f32_e32 v57, v54, v54
	v_fmac_f32_e32 v51, v55, v55
	v_fmac_f32_e32 v57, v56, v56
	v_add_f32_e32 v51, v57, v51
	v_and_b32_e32 v57, 0xffff0000, v62
	v_lshlrev_b32_e32 v58, 16, v62
	v_mul_f32_e32 v59, v57, v57
	v_fmac_f32_e32 v59, v58, v58
	v_add_f32_e32 v51, v59, v51
	v_and_b32_e32 v59, 0xffff0000, v63
	v_lshlrev_b32_e32 v61, 16, v63
	v_mul_f32_e32 v60, v59, v59
	v_fmac_f32_e32 v60, v61, v61
	v_add_f32_e32 v116, v60, v51
	s_waitcnt lgkmcnt(0)
	v_lshlrev_b32_e32 v162, 16, v144
	v_and_b32_e32 v152, 0xffff0000, v144
	v_lshlrev_b32_e32 v164, 16, v145
	v_and_b32_e32 v163, 0xffff0000, v145
	v_lshlrev_b32_e32 v166, 16, v146
	v_and_b32_e32 v165, 0xffff0000, v146
	v_lshlrev_b32_e32 v168, 16, v147
	v_and_b32_e32 v167, 0xffff0000, v147
	ds_read_b128 v[144:147], v0 offset:49920
	v_and_b32_e32 v60, 0xffff0000, v118
	v_and_b32_e32 v63, 0xffff0000, v119
	v_lshlrev_b32_e32 v62, 16, v118
	v_mul_f32_e32 v51, v60, v60
	v_lshlrev_b32_e32 v64, 16, v119
	v_mul_f32_e32 v65, v63, v63
	v_fmac_f32_e32 v51, v62, v62
	v_fmac_f32_e32 v65, v64, v64
	v_add_f32_e32 v51, v65, v51
	v_and_b32_e32 v65, 0xffff0000, v120
	v_lshlrev_b32_e32 v114, 16, v120
	v_mul_f32_e32 v115, v65, v65
	v_fmac_f32_e32 v115, v114, v114
	v_add_f32_e32 v51, v115, v51
	v_lshlrev_b32_e32 v123, 16, v121
	v_and_b32_e32 v115, 0xffff0000, v121
	ds_read_b128 v[118:121], v0 offset:16640
	v_mul_f32_e32 v117, v115, v115
	v_fmac_f32_e32 v117, v123, v123
	v_add_f32_e32 v117, v117, v51
	s_waitcnt lgkmcnt(1)
	v_and_b32_e32 v153, 0xffff0000, v144
	s_waitcnt lgkmcnt(0)
	v_and_b32_e32 v122, 0xffff0000, v118
	v_and_b32_e32 v124, 0xffff0000, v119
	v_lshlrev_b32_e32 v125, 16, v118
	v_mul_f32_e32 v51, v122, v122
	v_lshlrev_b32_e32 v126, 16, v119
	v_mul_f32_e32 v118, v124, v124
	v_fmac_f32_e32 v51, v125, v125
	v_fmac_f32_e32 v118, v126, v126
	v_and_b32_e32 v127, 0xffff0000, v120
	v_add_f32_e32 v51, v118, v51
	v_lshlrev_b32_e32 v128, 16, v120
	v_mul_f32_e32 v118, v127, v127
	v_fmac_f32_e32 v118, v128, v128
	v_and_b32_e32 v129, 0xffff0000, v121
	v_add_f32_e32 v51, v118, v51
	v_lshlrev_b32_e32 v131, 16, v121
	v_mul_f32_e32 v118, v129, v129
	v_fmac_f32_e32 v118, v131, v131
	v_add_f32_e32 v118, v118, v51
	v_mul_f32_e32 v51, v130, v130
	v_mul_f32_e32 v119, v133, v133
	v_fmac_f32_e32 v51, v132, v132
	v_fmac_f32_e32 v119, v134, v134
	v_add_f32_e32 v51, v119, v51
	v_mul_f32_e32 v119, v135, v135
	v_fmac_f32_e32 v119, v136, v136
	v_add_f32_e32 v51, v119, v51
	v_mul_f32_e32 v119, v137, v137
	v_fmac_f32_e32 v119, v139, v139
	v_add_f32_e32 v119, v119, v51
	v_mul_f32_e32 v51, v138, v138
	v_mul_f32_e32 v120, v140, v140
	v_fmac_f32_e32 v51, v141, v141
	v_fmac_f32_e32 v120, v142, v142
	v_add_f32_e32 v51, v120, v51
	v_mul_f32_e32 v120, v143, v143
	v_fmac_f32_e32 v120, v150, v150
	v_add_f32_e32 v51, v120, v51
	v_mul_f32_e32 v120, v151, v151
	v_fmac_f32_e32 v120, v161, v161
	v_add_f32_e32 v120, v120, v51
	v_mul_f32_e32 v51, v152, v152
	v_mul_f32_e32 v121, v163, v163
	v_fmac_f32_e32 v51, v162, v162
	v_fmac_f32_e32 v121, v164, v164
	v_add_f32_e32 v51, v121, v51
	v_mul_f32_e32 v121, v165, v165
	v_fmac_f32_e32 v121, v166, v166
	v_add_f32_e32 v51, v121, v51
	v_mul_f32_e32 v121, v167, v167
	v_fmac_f32_e32 v121, v168, v168
	v_and_b32_e32 v154, 0xffff0000, v145
	v_add_f32_e32 v169, v121, v51
	v_lshlrev_b32_e32 v155, 16, v144
	v_mul_f32_e32 v51, v153, v153
	v_lshlrev_b32_e32 v156, 16, v145
	v_mul_f32_e32 v121, v154, v154
	v_fmac_f32_e32 v51, v155, v155
	v_fmac_f32_e32 v121, v156, v156
	v_and_b32_e32 v157, 0xffff0000, v146
	v_add_f32_e32 v51, v121, v51
	v_lshlrev_b32_e32 v158, 16, v146
	v_mul_f32_e32 v121, v157, v157
	v_fmac_f32_e32 v121, v158, v158
	v_and_b32_e32 v159, 0xffff0000, v147
	v_add_f32_e32 v51, v121, v51
	v_lshlrev_b32_e32 v160, 16, v147
	v_mul_f32_e32 v121, v159, v159
	v_fmac_f32_e32 v121, v160, v160
	v_and_b32_e32 v0, 0xffff0000, v170
	v_and_b32_e32 v144, 0xffff0000, v171
	v_add_f32_e32 v174, v121, v51
	v_lshlrev_b32_e32 v51, 16, v170
	v_mul_f32_e32 v121, v0, v0
	v_lshlrev_b32_e32 v145, 16, v171
	v_mul_f32_e32 v146, v144, v144
	v_fmac_f32_e32 v121, v51, v51
	v_fmac_f32_e32 v146, v145, v145
	v_add_f32_e32 v121, v146, v121
	v_and_b32_e32 v146, 0xffff0000, v172
	v_lshlrev_b32_e32 v147, 16, v172
	v_mul_f32_e32 v148, v146, v146
	v_fmac_f32_e32 v148, v147, v147
	v_add_f32_e32 v121, v148, v121
	v_and_b32_e32 v148, 0xffff0000, v173
	v_lshlrev_b32_e32 v149, 16, v173
	v_mul_f32_e32 v170, v148, v148
	v_fmac_f32_e32 v170, v149, v149
	v_add_f32_e32 v170, v170, v121
	v_and_b32_e32 v121, 64, v234
	v_add_u32_e32 v171, 64, v121
	v_xor_b32_e32 v121, 1, v234
	v_cmp_lt_i32_e32 vcc, v121, v171
	s_addc_u32 s31, s29, 0
	v_cmp_eq_u32_e64 s[26:27], 0, v52
	v_cndmask_b32_e32 v121, v234, v121, vcc
	v_lshlrev_b32_e32 v121, 2, v121
	s_nop 1
	v_add_f32_dpp v116, v116, v116 quad_perm:[1,0,3,2] row_mask:0xf bank_mask:0xf
	s_nop 1
	v_add_f32_dpp v116, v116, v116 quad_perm:[2,3,0,1] row_mask:0xf bank_mask:0xf
	s_nop 1
	v_add_f32_dpp v116, v116, v116 row_half_mirror row_mask:0xf bank_mask:0xf
	s_nop 1
	v_add_f32_dpp v116, v116, v116 row_ror:8 row_mask:0xf bank_mask:0xf
	v_mov_b32_e32 v172, v116
	s_nop 1
	v_permlane16_swap_b32_e32 v116, v172
	s_nop 0
	v_add_f32_e32 v116, v116, v172
	v_mov_b32_e32 v172, v116
	s_nop 1
	v_permlane32_swap_b32_e32 v116, v172
	s_nop 0
	v_add_f32_e32 v116, v116, v172
	v_mov_b32_e32 v172, 0
	s_waitcnt lgkmcnt(0)
	v_add_f32_e32 v116, v116, v172
	s_nop 1
	v_add_f32_dpp v117, v117, v117 quad_perm:[1,0,3,2] row_mask:0xf bank_mask:0xf
	s_nop 1
	v_add_f32_dpp v117, v117, v117 quad_perm:[2,3,0,1] row_mask:0xf bank_mask:0xf
	s_nop 1
	v_add_f32_dpp v117, v117, v117 row_half_mirror row_mask:0xf bank_mask:0xf
	s_nop 1
	v_add_f32_dpp v117, v117, v117 row_ror:8 row_mask:0xf bank_mask:0xf
	v_mov_b32_e32 v172, v117
	s_nop 1
	v_permlane16_swap_b32_e32 v117, v172
	s_nop 0
	v_add_f32_e32 v117, v117, v172
	v_mov_b32_e32 v172, v117
	s_nop 1
	v_permlane32_swap_b32_e32 v117, v172
	s_nop 0
	v_add_f32_e32 v117, v117, v172
	v_mov_b32_e32 v172, 0
	s_waitcnt lgkmcnt(0)
	v_add_f32_e32 v117, v117, v172
	s_nop 1
	v_add_f32_dpp v118, v118, v118 quad_perm:[1,0,3,2] row_mask:0xf bank_mask:0xf
	s_nop 1
	v_add_f32_dpp v118, v118, v118 quad_perm:[2,3,0,1] row_mask:0xf bank_mask:0xf
	s_nop 1
	v_add_f32_dpp v118, v118, v118 row_half_mirror row_mask:0xf bank_mask:0xf
	s_nop 1
	v_add_f32_dpp v118, v118, v118 row_ror:8 row_mask:0xf bank_mask:0xf
	v_mov_b32_e32 v172, v118
	s_nop 1
	v_permlane16_swap_b32_e32 v118, v172
	s_nop 0
	v_add_f32_e32 v118, v118, v172
	v_mov_b32_e32 v172, v118
	s_nop 1
	v_permlane32_swap_b32_e32 v118, v172
	s_nop 0
	v_add_f32_e32 v118, v118, v172
	v_mov_b32_e32 v172, 0
	s_waitcnt lgkmcnt(0)
	v_add_f32_e32 v118, v118, v172
	s_nop 1
	v_add_f32_dpp v119, v119, v119 quad_perm:[1,0,3,2] row_mask:0xf bank_mask:0xf
	s_nop 1
	v_add_f32_dpp v119, v119, v119 quad_perm:[2,3,0,1] row_mask:0xf bank_mask:0xf
	s_nop 1
	v_add_f32_dpp v119, v119, v119 row_half_mirror row_mask:0xf bank_mask:0xf
	s_nop 1
	v_add_f32_dpp v119, v119, v119 row_ror:8 row_mask:0xf bank_mask:0xf
	v_mov_b32_e32 v172, v119
	s_nop 1
	v_permlane16_swap_b32_e32 v119, v172
	s_nop 0
	v_add_f32_e32 v119, v119, v172
	v_mov_b32_e32 v172, v119
	s_nop 1
	v_permlane32_swap_b32_e32 v119, v172
	s_nop 0
	v_add_f32_e32 v119, v119, v172
	v_mov_b32_e32 v172, 0
	s_waitcnt lgkmcnt(0)
	v_add_f32_e32 v119, v119, v172
	s_nop 1
	v_add_f32_dpp v120, v120, v120 quad_perm:[1,0,3,2] row_mask:0xf bank_mask:0xf
	s_nop 1
	v_add_f32_dpp v120, v120, v120 quad_perm:[2,3,0,1] row_mask:0xf bank_mask:0xf
	s_nop 1
	v_add_f32_dpp v120, v120, v120 row_half_mirror row_mask:0xf bank_mask:0xf
	s_nop 1
	v_add_f32_dpp v120, v120, v120 row_ror:8 row_mask:0xf bank_mask:0xf
	v_mov_b32_e32 v172, v120
	s_nop 1
	v_permlane16_swap_b32_e32 v120, v172
	s_nop 0
	v_add_f32_e32 v120, v120, v172
	v_mov_b32_e32 v172, v120
	s_nop 1
	v_permlane32_swap_b32_e32 v120, v172
	s_nop 0
	v_add_f32_e32 v120, v120, v172
	v_mov_b32_e32 v172, 0
	s_waitcnt lgkmcnt(0)
	v_add_f32_e32 v172, v120, v172
	s_nop 1
	v_add_f32_dpp v169, v169, v169 quad_perm:[1,0,3,2] row_mask:0xf bank_mask:0xf
	s_nop 1
	v_add_f32_dpp v169, v169, v169 quad_perm:[2,3,0,1] row_mask:0xf bank_mask:0xf
	s_nop 1
	v_add_f32_dpp v169, v169, v169 row_half_mirror row_mask:0xf bank_mask:0xf
	s_nop 1
	v_add_f32_dpp v169, v169, v169 row_ror:8 row_mask:0xf bank_mask:0xf
	v_mov_b32_e32 v120, v169
	s_nop 1
	v_permlane16_swap_b32_e32 v169, v120
	s_nop 0
	v_add_f32_e32 v169, v169, v120
	v_mov_b32_e32 v120, v169
	s_nop 1
	v_permlane32_swap_b32_e32 v169, v120
	s_nop 0
	v_add_f32_e32 v169, v169, v120
	v_mov_b32_e32 v120, 0
	s_waitcnt lgkmcnt(0)
	v_add_f32_e32 v169, v169, v120
	s_nop 1
	v_add_f32_dpp v174, v174, v174 quad_perm:[1,0,3,2] row_mask:0xf bank_mask:0xf
	s_nop 1
	v_add_f32_dpp v174, v174, v174 quad_perm:[2,3,0,1] row_mask:0xf bank_mask:0xf
	s_nop 1
	v_add_f32_dpp v174, v174, v174 row_half_mirror row_mask:0xf bank_mask:0xf
	s_nop 1
	v_add_f32_dpp v174, v174, v174 row_ror:8 row_mask:0xf bank_mask:0xf
	v_mov_b32_e32 v120, v174
	s_nop 1
	v_permlane16_swap_b32_e32 v174, v120
	s_nop 0
	v_add_f32_e32 v174, v174, v120
	v_mov_b32_e32 v120, v174
	s_nop 1
	v_permlane32_swap_b32_e32 v174, v120
	s_nop 0
	v_add_f32_e32 v174, v174, v120
	v_mov_b32_e32 v120, 0
	s_waitcnt lgkmcnt(0)
	v_add_f32_e32 v173, v174, v120
	s_nop 1
	v_add_f32_dpp v170, v170, v170 quad_perm:[1,0,3,2] row_mask:0xf bank_mask:0xf
	s_nop 1
	v_add_f32_dpp v170, v170, v170 quad_perm:[2,3,0,1] row_mask:0xf bank_mask:0xf
	s_nop 1
	v_add_f32_dpp v170, v170, v170 row_half_mirror row_mask:0xf bank_mask:0xf
	s_nop 1
	v_add_f32_dpp v170, v170, v170 row_ror:8 row_mask:0xf bank_mask:0xf
	v_mov_b32_e32 v120, v170
	s_nop 1
	v_permlane16_swap_b32_e32 v170, v120
	s_nop 0
	v_add_f32_e32 v170, v170, v120
	v_mov_b32_e32 v120, v170
	s_nop 1
	v_permlane32_swap_b32_e32 v170, v120
	s_nop 0
	v_add_f32_e32 v170, v170, v120
	v_mov_b32_e32 v120, 0
	s_waitcnt lgkmcnt(0)
	v_add_f32_e32 v170, v170, v120
	v_xor_b32_e32 v120, 2, v234
	v_cmp_lt_i32_e32 vcc, v120, v171
	s_nop 1
	v_cndmask_b32_e32 v120, v234, v120, vcc
	v_lshlrev_b32_e32 v120, 2, v120
	v_mov_b32_e32 v174, 0
	s_waitcnt lgkmcnt(0)
	v_add_f32_e32 v116, v116, v174
	v_mov_b32_e32 v174, 0
	s_waitcnt lgkmcnt(0)
	v_add_f32_e32 v117, v117, v174
	v_mov_b32_e32 v174, 0
	s_waitcnt lgkmcnt(0)
	v_add_f32_e32 v118, v118, v174
	v_mov_b32_e32 v174, 0
	s_waitcnt lgkmcnt(0)
	v_add_f32_e32 v174, v119, v174
	v_mov_b32_e32 v119, 0
	s_waitcnt lgkmcnt(0)
	v_add_f32_e32 v172, v172, v119
	v_mov_b32_e32 v119, 0
	s_waitcnt lgkmcnt(0)
	v_add_f32_e32 v169, v169, v119
	v_mov_b32_e32 v119, 0
	s_waitcnt lgkmcnt(0)
	v_add_f32_e32 v173, v173, v119
	v_mov_b32_e32 v119, 0
	s_waitcnt lgkmcnt(0)
	v_add_f32_e32 v170, v170, v119
	v_xor_b32_e32 v119, 4, v234
	v_cmp_lt_i32_e32 vcc, v119, v171
	s_nop 1
	v_cndmask_b32_e32 v119, v234, v119, vcc
	v_lshlrev_b32_e32 v119, 2, v119
	v_mov_b32_e32 v175, 0
	s_waitcnt lgkmcnt(0)
	v_add_f32_e32 v116, v116, v175
	v_mov_b32_e32 v175, 0
	s_waitcnt lgkmcnt(0)
	v_add_f32_e32 v117, v117, v175
	v_mov_b32_e32 v175, 0
	s_waitcnt lgkmcnt(0)
	v_add_f32_e32 v175, v118, v175
	v_mov_b32_e32 v118, 0
	s_waitcnt lgkmcnt(0)
	v_add_f32_e32 v174, v174, v118
	v_mov_b32_e32 v118, 0
	s_waitcnt lgkmcnt(0)
	v_add_f32_e32 v172, v172, v118
	v_mov_b32_e32 v118, 0
	s_waitcnt lgkmcnt(0)
	v_add_f32_e32 v169, v169, v118
	v_mov_b32_e32 v118, 0
	s_waitcnt lgkmcnt(0)
	v_add_f32_e32 v173, v173, v118
	v_mov_b32_e32 v118, 0
	s_waitcnt lgkmcnt(0)
	v_add_f32_e32 v170, v170, v118
	v_xor_b32_e32 v118, 8, v234
	v_cmp_lt_i32_e32 vcc, v118, v171
	s_nop 1
	v_cndmask_b32_e32 v118, v234, v118, vcc
	v_lshlrev_b32_e32 v118, 2, v118
	v_mov_b32_e32 v176, 0
	s_waitcnt lgkmcnt(0)
	v_add_f32_e32 v176, v116, v176
	v_mov_b32_e32 v116, 0
	s_waitcnt lgkmcnt(0)
	v_add_f32_e32 v117, v117, v116
	v_mov_b32_e32 v116, 0
	s_waitcnt lgkmcnt(0)
	v_add_f32_e32 v175, v175, v116
	v_mov_b32_e32 v116, 0
	s_waitcnt lgkmcnt(0)
	v_add_f32_e32 v174, v174, v116
	v_mov_b32_e32 v116, 0
	s_waitcnt lgkmcnt(0)
	v_add_f32_e32 v172, v172, v116
	v_mov_b32_e32 v116, 0
	s_waitcnt lgkmcnt(0)
	v_add_f32_e32 v169, v169, v116
	v_mov_b32_e32 v116, 0
	s_waitcnt lgkmcnt(0)
	v_add_f32_e32 v173, v173, v116
	v_mov_b32_e32 v116, 0
	s_waitcnt lgkmcnt(0)
	v_add_f32_e32 v170, v170, v116
	v_xor_b32_e32 v116, 16, v234
	v_cmp_lt_i32_e32 vcc, v116, v171
	s_nop 1
	v_cndmask_b32_e32 v116, v234, v116, vcc
	v_lshlrev_b32_e32 v116, 2, v116
	v_mov_b32_e32 v177, 0
	s_waitcnt lgkmcnt(0)
	v_add_f32_e32 v176, v176, v177
	v_mov_b32_e32 v177, 0
	s_waitcnt lgkmcnt(0)
	v_add_f32_e32 v177, v117, v177
	v_mov_b32_e32 v117, 0
	s_waitcnt lgkmcnt(0)
	v_add_f32_e32 v175, v175, v117
	v_mov_b32_e32 v117, 0
	s_waitcnt lgkmcnt(0)
	v_add_f32_e32 v174, v174, v117
	v_mov_b32_e32 v117, 0
	s_waitcnt lgkmcnt(0)
	v_add_f32_e32 v172, v172, v117
	v_mov_b32_e32 v117, 0
	s_waitcnt lgkmcnt(0)
	v_add_f32_e32 v169, v169, v117
	v_mov_b32_e32 v117, 0
	s_waitcnt lgkmcnt(0)
	v_add_f32_e32 v178, v173, v117
	v_mov_b32_e32 v117, 0
	s_waitcnt lgkmcnt(0)
	v_add_f32_e32 v179, v170, v117
	v_xor_b32_e32 v117, 32, v234
	v_cmp_lt_i32_e32 vcc, v117, v171
	s_nop 1
	v_cndmask_b32_e32 v117, v234, v117, vcc
	v_lshlrev_b32_e32 v117, 2, v117
	v_mov_b32_e32 v170, 0
	s_waitcnt lgkmcnt(0)
	v_add_f32_e32 v176, v176, v170
	v_mov_b32_e32 v170, 0
	s_waitcnt lgkmcnt(0)
	v_add_f32_e32 v177, v177, v170
	v_mov_b32_e32 v170, 0
	s_waitcnt lgkmcnt(0)
	v_add_f32_e32 v175, v175, v170
	v_mov_b32_e32 v170, 0
	s_waitcnt lgkmcnt(0)
	v_add_f32_e32 v173, v174, v170
	v_mov_b32_e32 v170, 0
	v_fmamk_f32 v174, v176, 0x3b000000, v235
	v_rsq_f32_e32 v174, v174
	v_fmamk_f32 v173, v173, 0x3b000000, v235
	v_rsq_f32_e32 v173, v173
	s_waitcnt lgkmcnt(0)
	v_add_f32_e32 v172, v172, v170
	v_mov_b32_e32 v170, 0
	v_mul_f32_e32 v53, v174, v53
	s_waitcnt vmcnt(0)
	v_mul_f32_e32 v176, v47, v53
	v_mul_f32_e32 v53, v174, v56
	v_mul_f32_e32 v56, v48, v53
	s_waitcnt lgkmcnt(0)
	v_add_f32_e32 v171, v169, v170
	v_mov_b32_e32 v169, 0
	v_mul_f32_e32 v53, v174, v54
	v_mul_f32_e32 v55, v174, v55
	v_mul_f32_e32 v55, v46, v55
	v_mul_f32_e32 v54, 0xbfb8aa3b, v176
	s_waitcnt lgkmcnt(0)
	v_add_f32_e32 v170, v178, v169
	v_mov_b32_e32 v169, 0
	v_mul_f32_e32 v178, v49, v53
	v_mul_f32_e32 v53, v174, v58
	v_mul_f32_e32 v58, v42, v53
	v_mul_f32_e32 v53, v174, v57
	s_waitcnt lgkmcnt(0)
	v_add_f32_e32 v169, v179, v169
	v_mul_f32_e32 v179, v43, v53
	v_mul_f32_e32 v53, v174, v61
	v_mul_f32_e32 v61, v44, v53
	v_mul_f32_e32 v53, v174, v59
	v_mul_f32_e32 v174, v45, v53
	v_mul_f32_e32 v53, 0xbfb8aa3b, v55
	v_mul_f32_e32 v59, 0xbfb8aa3b, v61
	v_exp_f32_e32 v53, v53
	v_exp_f32_e32 v59, v59
	v_exp_f32_e32 v54, v54
	v_mul_f32_e32 v130, v173, v130
	v_add_f32_e32 v53, 1.0, v53
	v_add_f32_e32 v59, 1.0, v59
	v_rcp_f32_e32 v53, v53
	v_rcp_f32_e32 v59, v59
	v_add_f32_e32 v54, 1.0, v54
	v_rcp_f32_e32 v54, v54
	v_mul_f32_e32 v53, v55, v53
	v_mul_f32_e32 v55, 0xbfb8aa3b, v56
	v_mul_f32_e32 v59, v61, v59
	v_mul_f32_e32 v61, 0xbfb8aa3b, v174
	v_exp_f32_e32 v55, v55
	v_exp_f32_e32 v61, v61
	v_mul_f32_e32 v54, v176, v54
	v_mul_f32_e32 v132, v173, v132
	v_add_f32_e32 v55, 1.0, v55
	v_add_f32_e32 v61, 1.0, v61
	v_rcp_f32_e32 v55, v55
	v_rcp_f32_e32 v61, v61
	v_mul_f32_e32 v132, v46, v132
	v_fmamk_f32 v172, v172, 0x3b000000, v235
	v_mul_f32_e32 v55, v56, v55
	v_mul_f32_e32 v56, 0xbfb8aa3b, v178
	v_mul_f32_e32 v61, v174, v61
	v_fmamk_f32 v174, v177, 0x3b000000, v235
	v_exp_f32_e32 v56, v56
	v_rsq_f32_e32 v174, v174
	v_rsq_f32_e32 v172, v172
	v_fmamk_f32 v171, v171, 0x3b000000, v235
	v_add_f32_e32 v56, 1.0, v56
	v_mul_f32_e32 v60, v174, v60
	v_rcp_f32_e32 v56, v56
	v_mul_f32_e32 v176, v47, v60
	v_mul_f32_e32 v60, v174, v64
	v_mul_f32_e32 v64, v48, v60
	v_mul_f32_e32 v60, v174, v63
	v_mul_f32_e32 v177, v49, v60
	v_mul_f32_e32 v60, v174, v114
	v_mul_f32_e32 v114, v42, v60
	v_mul_f32_e32 v60, v174, v65
	v_mul_f32_e32 v56, v178, v56
	v_mul_f32_e32 v178, v43, v60
	v_mul_f32_e32 v60, v174, v123
	v_mul_f32_e32 v123, v44, v60
	v_mul_f32_e32 v60, v174, v115
	v_mul_f32_e32 v115, 0xbfb8aa3b, v123
	v_exp_f32_e32 v115, v115
	v_mul_f32_e32 v62, v174, v62
	v_mul_f32_e32 v62, v46, v62
	v_mul_f32_e32 v174, v45, v60
	v_add_f32_e32 v115, 1.0, v115
	v_rcp_f32_e32 v115, v115
	v_mul_f32_e32 v60, 0xbfb8aa3b, v62
	v_exp_f32_e32 v60, v60
	v_mul_f32_e32 v63, 0xbfb8aa3b, v64
	v_mul_f32_e32 v115, v123, v115
	v_mul_f32_e32 v123, 0xbfb8aa3b, v174
	v_exp_f32_e32 v63, v63
	v_exp_f32_e32 v123, v123
	v_add_f32_e32 v60, 1.0, v60
	v_rcp_f32_e32 v60, v60
	v_add_f32_e32 v63, 1.0, v63
	v_add_f32_e32 v123, 1.0, v123
	v_rcp_f32_e32 v63, v63
	v_rcp_f32_e32 v123, v123
	v_mul_f32_e32 v60, v62, v60
	v_mul_f32_e32 v62, 0xbfb8aa3b, v176
	v_exp_f32_e32 v62, v62
	v_mul_f32_e32 v63, v64, v63
	v_mul_f32_e32 v64, 0xbfb8aa3b, v177
	v_mul_f32_e32 v123, v174, v123
	v_fmamk_f32 v174, v175, 0x3b000000, v235
	v_exp_f32_e32 v64, v64
	v_rsq_f32_e32 v174, v174
	v_add_f32_e32 v62, 1.0, v62
	v_rcp_f32_e32 v62, v62
	v_add_f32_e32 v64, 1.0, v64
	v_mul_f32_e32 v122, v174, v122
	v_rcp_f32_e32 v64, v64
	v_mul_f32_e32 v175, v47, v122
	v_mul_f32_e32 v122, v174, v126
	v_mul_f32_e32 v126, v48, v122
	v_mul_f32_e32 v122, v174, v124
	v_mul_f32_e32 v62, v176, v62
	v_mul_f32_e32 v176, v49, v122
	v_mul_f32_e32 v122, v174, v128
	v_mul_f32_e32 v128, v42, v122
	v_mul_f32_e32 v122, v174, v127
	v_mul_f32_e32 v64, v177, v64
	v_mul_f32_e32 v125, v174, v125
	v_mul_f32_e32 v177, v43, v122
	v_mul_f32_e32 v122, v174, v131
	v_mul_f32_e32 v125, v46, v125
	v_mul_f32_e32 v131, v44, v122
	v_mul_f32_e32 v122, v174, v129
	v_mul_f32_e32 v174, v45, v122
	v_mul_f32_e32 v122, 0xbfb8aa3b, v125
	v_exp_f32_e32 v122, v122
	v_mul_f32_e32 v129, 0xbfb8aa3b, v131
	v_exp_f32_e32 v129, v129
	v_mul_f32_e32 v124, 0xbfb8aa3b, v175
	v_add_f32_e32 v122, 1.0, v122
	v_rcp_f32_e32 v122, v122
	v_add_f32_e32 v129, 1.0, v129
	v_rcp_f32_e32 v129, v129
	v_exp_f32_e32 v124, v124
	v_mul_f32_e32 v122, v125, v122
	v_mul_f32_e32 v125, 0xbfb8aa3b, v126
	v_exp_f32_e32 v125, v125
	v_mul_f32_e32 v129, v131, v129
	v_mul_f32_e32 v131, 0xbfb8aa3b, v174
	v_exp_f32_e32 v131, v131
	v_add_f32_e32 v125, 1.0, v125
	v_rcp_f32_e32 v125, v125
	v_add_f32_e32 v124, 1.0, v124
	v_add_f32_e32 v131, 1.0, v131
	v_rcp_f32_e32 v131, v131
	v_mul_f32_e32 v125, v126, v125
	v_mul_f32_e32 v126, 0xbfb8aa3b, v176
	v_exp_f32_e32 v126, v126
	v_rcp_f32_e32 v124, v124
	v_mul_f32_e32 v131, v174, v131
	v_mul_f32_e32 v174, v47, v130
	v_add_f32_e32 v126, 1.0, v126
	v_rcp_f32_e32 v126, v126
	v_mul_f32_e32 v130, v173, v134
	v_mul_f32_e32 v134, v48, v130
	v_mul_f32_e32 v130, v173, v133
	v_mul_f32_e32 v124, v175, v124
	v_mul_f32_e32 v175, v49, v130
	v_mul_f32_e32 v130, v173, v136
	v_mul_f32_e32 v136, v42, v130
	v_mul_f32_e32 v130, v173, v135
	v_mul_f32_e32 v126, v176, v126
	v_mul_f32_e32 v176, v43, v130
	v_mul_f32_e32 v130, v173, v139
	v_mul_f32_e32 v139, v44, v130
	v_mul_f32_e32 v130, v173, v137
	v_mul_f32_e32 v137, 0xbfb8aa3b, v139
	v_exp_f32_e32 v137, v137
	v_mul_f32_e32 v173, v45, v130
	v_mul_f32_e32 v130, 0xbfb8aa3b, v132
	v_exp_f32_e32 v130, v130
	v_mul_f32_e32 v133, 0xbfb8aa3b, v134
	v_exp_f32_e32 v133, v133
	v_add_f32_e32 v137, 1.0, v137
	v_rcp_f32_e32 v137, v137
	v_add_f32_e32 v130, 1.0, v130
	v_rcp_f32_e32 v130, v130
	v_add_f32_e32 v133, 1.0, v133
	v_rcp_f32_e32 v133, v133
	v_mul_f32_e32 v137, v139, v137
	v_mul_f32_e32 v139, 0xbfb8aa3b, v173
	v_exp_f32_e32 v139, v139
	v_mul_f32_e32 v130, v132, v130
	v_mul_f32_e32 v132, 0xbfb8aa3b, v174
	v_exp_f32_e32 v132, v132
	v_mul_f32_e32 v133, v134, v133
	v_mul_f32_e32 v134, 0xbfb8aa3b, v175
	v_exp_f32_e32 v134, v134
	v_add_f32_e32 v139, 1.0, v139
	v_rcp_f32_e32 v139, v139
	v_add_f32_e32 v132, 1.0, v132
	v_rcp_f32_e32 v132, v132
	v_add_f32_e32 v134, 1.0, v134
	v_mul_f32_e32 v138, v172, v138
	v_rcp_f32_e32 v134, v134
	v_mul_f32_e32 v139, v173, v139
	v_mul_f32_e32 v173, v47, v138
	v_mul_f32_e32 v138, v172, v142
	v_mul_f32_e32 v142, v48, v138
	v_mul_f32_e32 v138, v172, v140
	v_mul_f32_e32 v132, v174, v132
	v_mul_f32_e32 v174, v49, v138
	v_mul_f32_e32 v138, v172, v150
	v_mul_f32_e32 v150, v42, v138
	v_mul_f32_e32 v138, v172, v143
	v_mul_f32_e32 v134, v175, v134
	v_mul_f32_e32 v141, v172, v141
	v_mul_f32_e32 v175, v43, v138
	v_mul_f32_e32 v138, v172, v161
	v_mul_f32_e32 v141, v46, v141
	v_mul_f32_e32 v161, v44, v138
	v_mul_f32_e32 v138, v172, v151
	v_mul_f32_e32 v172, v45, v138
	v_mul_f32_e32 v138, 0xbfb8aa3b, v141
	v_exp_f32_e32 v138, v138
	v_mul_f32_e32 v151, 0xbfb8aa3b, v161
	v_exp_f32_e32 v151, v151
	v_mul_f32_e32 v140, 0xbfb8aa3b, v173
	v_add_f32_e32 v138, 1.0, v138
	v_rcp_f32_e32 v138, v138
	v_add_f32_e32 v151, 1.0, v151
	v_rcp_f32_e32 v151, v151
	v_exp_f32_e32 v140, v140
	v_mul_f32_e32 v138, v141, v138
	v_mul_f32_e32 v141, 0xbfb8aa3b, v142
	v_exp_f32_e32 v141, v141
	v_mul_f32_e32 v151, v161, v151
	v_mul_f32_e32 v161, 0xbfb8aa3b, v172
	v_exp_f32_e32 v161, v161
	v_add_f32_e32 v141, 1.0, v141
	v_rcp_f32_e32 v141, v141
	v_rsq_f32_e32 v171, v171
	v_add_f32_e32 v161, 1.0, v161
	v_rcp_f32_e32 v161, v161
	v_mul_f32_e32 v141, v142, v141
	v_mul_f32_e32 v142, 0xbfb8aa3b, v174
	v_exp_f32_e32 v142, v142
	v_add_f32_e32 v140, 1.0, v140
	v_rcp_f32_e32 v140, v140
	v_mul_f32_e32 v152, v171, v152
	v_add_f32_e32 v142, 1.0, v142
	v_rcp_f32_e32 v142, v142
	v_mul_f32_e32 v161, v172, v161
	v_mul_f32_e32 v172, v47, v152
	v_mul_f32_e32 v152, v171, v164
	v_mul_f32_e32 v164, v48, v152
	v_mul_f32_e32 v152, v171, v163
	v_mul_f32_e32 v140, v173, v140
	v_mul_f32_e32 v173, v49, v152
	v_mul_f32_e32 v152, v171, v166
	v_mul_f32_e32 v166, v42, v152
	v_mul_f32_e32 v152, v171, v165
	v_mul_f32_e32 v142, v174, v142
	v_mul_f32_e32 v174, v43, v152
	v_mul_f32_e32 v152, v171, v168
	v_mul_f32_e32 v168, v44, v152
	v_mul_f32_e32 v162, v171, v162
	v_mul_f32_e32 v152, v171, v167
	v_mul_f32_e32 v167, 0xbfb8aa3b, v168
	v_mul_f32_e32 v162, v46, v162
	v_exp_f32_e32 v167, v167
	v_mul_f32_e32 v171, v45, v152
	v_mul_f32_e32 v152, 0xbfb8aa3b, v162
	v_exp_f32_e32 v152, v152
	v_mul_f32_e32 v163, 0xbfb8aa3b, v164
	v_exp_f32_e32 v163, v163
	v_add_f32_e32 v167, 1.0, v167
	v_rcp_f32_e32 v167, v167
	v_add_f32_e32 v152, 1.0, v152
	v_rcp_f32_e32 v152, v152
	v_add_f32_e32 v163, 1.0, v163
	v_rcp_f32_e32 v163, v163
	v_mul_f32_e32 v167, v168, v167
	v_mul_f32_e32 v168, 0xbfb8aa3b, v171
	v_exp_f32_e32 v168, v168
	v_mul_f32_e32 v152, v162, v152
	v_mul_f32_e32 v162, 0xbfb8aa3b, v172
	v_exp_f32_e32 v162, v162
	v_mul_f32_e32 v163, v164, v163
	v_mul_f32_e32 v164, 0xbfb8aa3b, v173
	v_fmamk_f32 v170, v170, 0x3b000000, v235
	v_fmamk_f32 v169, v169, 0x3b000000, v235
	v_exp_f32_e32 v164, v164
	v_add_f32_e32 v168, 1.0, v168
	v_rsq_f32_e32 v170, v170
	v_rsq_f32_e32 v169, v169
	v_rcp_f32_e32 v168, v168
	v_add_f32_e32 v162, 1.0, v162
	v_rcp_f32_e32 v162, v162
	v_add_f32_e32 v164, 1.0, v164
	v_mul_f32_e32 v153, v170, v153
	v_mul_f32_e32 v0, v169, v0
	v_rcp_f32_e32 v164, v164
	v_mul_f32_e32 v168, v171, v168
	v_mul_f32_e32 v171, v47, v153
	v_mul_f32_e32 v153, v170, v156
	v_mul_f32_e32 v0, v47, v0
	v_mul_f32_e32 v47, v169, v145
	v_mul_f32_e32 v155, v170, v155
	v_mul_f32_e32 v156, v48, v153
	v_mul_f32_e32 v153, v170, v154
	v_mul_f32_e32 v51, v169, v51
	v_mul_f32_e32 v47, v48, v47
	v_mul_f32_e32 v48, v169, v144
	v_mul_f32_e32 v162, v172, v162
	v_mul_f32_e32 v155, v46, v155
	v_mul_f32_e32 v172, v49, v153
	v_mul_f32_e32 v153, v170, v158
	v_mul_f32_e32 v46, v46, v51
	v_mul_f32_e32 v51, v49, v48
	v_mul_f32_e32 v48, v169, v147
	v_mul_f32_e32 v158, v42, v153
	v_mul_f32_e32 v153, v170, v157
	v_mul_f32_e32 v42, v42, v48
	v_mul_f32_e32 v48, v169, v146
	v_mul_f32_e32 v164, v173, v164
	v_mul_f32_e32 v173, v43, v153
	v_mul_f32_e32 v153, v170, v160
	v_mul_f32_e32 v43, v43, v48
	v_mul_f32_e32 v48, v169, v149
	v_mul_f32_e32 v160, v44, v153
	v_mul_f32_e32 v153, v170, v159
	v_mul_f32_e32 v44, v44, v48
	v_mul_f32_e32 v48, v169, v148
	v_mul_f32_e32 v170, v45, v153
	v_mul_f32_e32 v45, v45, v48
	v_mul_f32_e32 v48, 0xbfb8aa3b, v46
	v_exp_f32_e32 v48, v48
	v_mul_f32_e32 v57, 0xbfb8aa3b, v58
	v_exp_f32_e32 v57, v57
	v_mul_f32_e32 v65, 0xbfb8aa3b, v114
	v_add_f32_e32 v48, 1.0, v48
	v_rcp_f32_e32 v48, v48
	v_add_f32_e32 v57, 1.0, v57
	v_rcp_f32_e32 v57, v57
	v_exp_f32_e32 v65, v65
	v_mul_f32_e32 v48, v46, v48
	v_mul_f32_e32 v46, 0xbfb8aa3b, v0
	v_exp_f32_e32 v46, v46
	v_mul_f32_e32 v57, v58, v57
	v_mul_f32_e32 v58, 0xbfb8aa3b, v179
	v_exp_f32_e32 v58, v58
	v_add_f32_e32 v46, 1.0, v46
	v_rcp_f32_e32 v46, v46
	v_add_f32_e32 v65, 1.0, v65
	v_rcp_f32_e32 v65, v65
	v_mul_f32_e32 v127, 0xbfb8aa3b, v128
	v_mul_f32_e32 v49, v0, v46
	v_mul_f32_e32 v0, 0xbfb8aa3b, v47
	v_exp_f32_e32 v0, v0
	v_exp_f32_e32 v127, v127
	v_add_f32_e32 v58, 1.0, v58
	v_rcp_f32_e32 v58, v58
	v_add_f32_e32 v0, 1.0, v0
	v_rcp_f32_e32 v0, v0
	v_mul_f32_e32 v65, v114, v65
	v_mul_f32_e32 v114, 0xbfb8aa3b, v178
	v_exp_f32_e32 v114, v114
	v_mul_f32_e32 v144, v47, v0
	v_mul_f32_e32 v0, 0xbfb8aa3b, v51
	v_exp_f32_e32 v0, v0
	v_add_f32_e32 v127, 1.0, v127
	v_rcp_f32_e32 v127, v127
	v_mul_f32_e32 v135, 0xbfb8aa3b, v136
	v_add_f32_e32 v0, 1.0, v0
	v_rcp_f32_e32 v0, v0
	v_exp_f32_e32 v135, v135
	v_mul_f32_e32 v58, v179, v58
	v_add_f32_e32 v114, 1.0, v114
	v_mul_f32_e32 v146, v51, v0
	v_mul_f32_e32 v0, 0xbfb8aa3b, v42
	v_exp_f32_e32 v0, v0
	v_rcp_f32_e32 v114, v114
	v_mul_f32_e32 v127, v128, v127
	v_mul_f32_e32 v128, 0xbfb8aa3b, v177
	v_add_f32_e32 v0, 1.0, v0
	v_rcp_f32_e32 v0, v0
	v_exp_f32_e32 v128, v128
	v_add_f32_e32 v135, 1.0, v135
	v_rcp_f32_e32 v135, v135
	v_mul_f32_e32 v145, v42, v0
	v_mul_f32_e32 v0, 0xbfb8aa3b, v43
	v_exp_f32_e32 v0, v0
	v_mul_f32_e32 v143, 0xbfb8aa3b, v150
	v_exp_f32_e32 v143, v143
	v_mul_f32_e32 v153, 0xbfb8aa3b, v155
	v_add_f32_e32 v0, 1.0, v0
	v_rcp_f32_e32 v0, v0
	v_max3_f32 v42, |v60|, 0, |v62|
	v_mul_f32_e32 v114, v178, v114
	v_exp_f32_e32 v153, v153
	v_mul_f32_e32 v147, v43, v0
	v_mul_f32_e32 v0, 0xbfb8aa3b, v44
	v_exp_f32_e32 v0, v0
	v_max3_f32 v42, v42, |v63|, |v64|
	v_add_f32_e32 v128, 1.0, v128
	v_max3_f32 v42, v42, |v65|, |v114|
	v_add_f32_e32 v0, 1.0, v0
	v_rcp_f32_e32 v0, v0
	v_rcp_f32_e32 v128, v128
	v_mul_f32_e32 v135, v136, v135
	v_mul_f32_e32 v136, 0xbfb8aa3b, v176
	v_mul_f32_e32 v148, v44, v0
	v_mul_f32_e32 v0, 0xbfb8aa3b, v45
	v_exp_f32_e32 v0, v0
	v_max3_f32 v42, v42, |v115|, |v123|
	v_exp_f32_e32 v136, v136
	v_add_f32_e32 v143, 1.0, v143
	v_add_f32_e32 v0, 1.0, v0
	v_rcp_f32_e32 v0, v0
	v_rcp_f32_e32 v143, v143
	v_mul_f32_e32 v165, 0xbfb8aa3b, v166
	v_add_f32_e32 v153, 1.0, v153
	v_mul_f32_e32 v149, v45, v0
	v_max3_f32 v0, |v53|, 0, |v54|
	v_max3_f32 v0, v0, |v55|, |v56|
	v_max3_f32 v0, v0, |v57|, |v58|
	v_max3_f32 v0, v0, |v59|, |v61|
	s_nop 1
	v_max_f32_dpp v0, v0, v0 quad_perm:[1,0,3,2] row_mask:0xf bank_mask:0xf
	s_nop 1
	v_max_f32_dpp v0, v0, v0 quad_perm:[2,3,0,1] row_mask:0xf bank_mask:0xf
	s_nop 1
	v_max_f32_dpp v0, v0, v0 row_half_mirror row_mask:0xf bank_mask:0xf
	s_nop 1
	v_max_f32_dpp v0, v0, v0 row_ror:8 row_mask:0xf bank_mask:0xf
	v_mov_b32_e32 v169, v0
	s_nop 1
	v_permlane16_swap_b32_e32 v0, v169
	s_nop 0
	v_max_f32_e32 v0, v0, v169
	v_mov_b32_e32 v169, v0
	s_nop 1
	v_permlane32_swap_b32_e32 v0, v169
	s_nop 0
	v_max_f32_e32 v0, v0, v169
	v_mov_b32_e32 v169, v0
	v_exp_f32_e32 v165, v165
	v_rcp_f32_e32 v153, v153
	v_max3_f32 v43, |v122|, 0, |v124|
	v_mul_f32_e32 v128, v177, v128
	s_waitcnt lgkmcnt(0)
	v_max_f32_e32 v169, v169, v169
	v_max_f32_e32 v0, v0, v169
	s_nop 1
	v_max_f32_dpp v42, v42, v42 quad_perm:[1,0,3,2] row_mask:0xf bank_mask:0xf
	s_nop 1
	v_max_f32_dpp v42, v42, v42 quad_perm:[2,3,0,1] row_mask:0xf bank_mask:0xf
	s_nop 1
	v_max_f32_dpp v42, v42, v42 row_half_mirror row_mask:0xf bank_mask:0xf
	s_nop 1
	v_max_f32_dpp v42, v42, v42 row_ror:8 row_mask:0xf bank_mask:0xf
	v_mov_b32_e32 v169, v42
	s_nop 1
	v_permlane16_swap_b32_e32 v42, v169
	s_nop 0
	v_max_f32_e32 v42, v42, v169
	v_mov_b32_e32 v169, v42
	s_nop 1
	v_permlane32_swap_b32_e32 v42, v169
	s_nop 0
	v_max_f32_e32 v42, v42, v169
	v_mov_b32_e32 v169, v42
	v_max3_f32 v43, v43, |v125|, |v126|
	v_add_f32_e32 v136, 1.0, v136
	v_max3_f32 v43, v43, |v127|, |v128|
	v_rcp_f32_e32 v136, v136
	v_mul_f32_e32 v143, v150, v143
	v_mul_f32_e32 v150, 0xbfb8aa3b, v175
	v_max3_f32 v43, v43, |v129|, |v131|
	s_waitcnt lgkmcnt(0)
	v_max_f32_e32 v169, v169, v169
	v_exp_f32_e32 v150, v150
	v_add_f32_e32 v165, 1.0, v165
	v_mul_f32_e32 v153, v155, v153
	v_mul_f32_e32 v155, 0xbfb8aa3b, v156
	v_max_f32_e32 v42, v42, v169
	s_nop 1
	v_max_f32_dpp v43, v43, v43 quad_perm:[1,0,3,2] row_mask:0xf bank_mask:0xf
	s_nop 1
	v_max_f32_dpp v43, v43, v43 quad_perm:[2,3,0,1] row_mask:0xf bank_mask:0xf
	s_nop 1
	v_max_f32_dpp v43, v43, v43 row_half_mirror row_mask:0xf bank_mask:0xf
	s_nop 1
	v_max_f32_dpp v43, v43, v43 row_ror:8 row_mask:0xf bank_mask:0xf
	v_mov_b32_e32 v169, v43
	s_nop 1
	v_permlane16_swap_b32_e32 v43, v169
	s_nop 0
	v_max_f32_e32 v43, v43, v169
	v_mov_b32_e32 v169, v43
	s_nop 1
	v_permlane32_swap_b32_e32 v43, v169
	s_nop 0
	v_max_f32_e32 v43, v43, v169
	v_mov_b32_e32 v169, v43
	v_rcp_f32_e32 v165, v165
	v_exp_f32_e32 v155, v155
	v_mul_f32_e32 v157, 0xbfb8aa3b, v158
	v_exp_f32_e32 v157, v157
	v_mul_f32_e32 v159, 0xbfb8aa3b, v160
	v_max3_f32 v44, |v130|, 0, |v132|
	v_mul_f32_e32 v136, v176, v136
	v_exp_f32_e32 v159, v159
	v_max3_f32 v44, v44, |v133|, |v134|
	v_add_f32_e32 v150, 1.0, v150
	v_max3_f32 v44, v44, |v135|, |v136|
	v_rcp_f32_e32 v150, v150
	v_mul_f32_e32 v165, v166, v165
	v_mul_f32_e32 v166, 0xbfb8aa3b, v174
	v_add_f32_e32 v155, 1.0, v155
	v_max3_f32 v44, v44, |v137|, |v139|
	s_waitcnt lgkmcnt(0)
	v_max_f32_e32 v169, v169, v169
	v_exp_f32_e32 v166, v166
	v_rcp_f32_e32 v155, v155
	v_add_f32_e32 v157, 1.0, v157
	v_max_f32_e32 v43, v43, v169
	s_nop 1
	v_max_f32_dpp v44, v44, v44 quad_perm:[1,0,3,2] row_mask:0xf bank_mask:0xf
	s_nop 1
	v_max_f32_dpp v44, v44, v44 quad_perm:[2,3,0,1] row_mask:0xf bank_mask:0xf
	s_nop 1
	v_max_f32_dpp v44, v44, v44 row_half_mirror row_mask:0xf bank_mask:0xf
	s_nop 1
	v_max_f32_dpp v44, v44, v44 row_ror:8 row_mask:0xf bank_mask:0xf
	v_mov_b32_e32 v169, v44
	s_nop 1
	v_permlane16_swap_b32_e32 v44, v169
	s_nop 0
	v_max_f32_e32 v44, v44, v169
	v_mov_b32_e32 v169, v44
	s_nop 1
	v_permlane32_swap_b32_e32 v44, v169
	s_nop 0
	v_max_f32_e32 v44, v44, v169
	v_mov_b32_e32 v169, v44
	v_rcp_f32_e32 v157, v157
	v_add_f32_e32 v159, 1.0, v159
	v_rcp_f32_e32 v159, v159
	v_max3_f32 v45, |v138|, 0, |v140|
	v_mul_f32_e32 v150, v175, v150
	v_mul_f32_e32 v154, 0xbfb8aa3b, v171
	v_max3_f32 v45, v45, |v141|, |v142|
	v_add_f32_e32 v166, 1.0, v166
	v_exp_f32_e32 v154, v154
	v_mul_f32_e32 v155, v156, v155
	v_mul_f32_e32 v156, 0xbfb8aa3b, v172
	v_max3_f32 v45, v45, |v143|, |v150|
	v_rcp_f32_e32 v166, v166
	v_exp_f32_e32 v156, v156
	v_mul_f32_e32 v157, v158, v157
	v_mul_f32_e32 v158, 0xbfb8aa3b, v173
	v_max3_f32 v45, v45, |v151|, |v161|
	s_waitcnt lgkmcnt(0)
	v_max_f32_e32 v169, v169, v169
	v_exp_f32_e32 v158, v158
	v_mul_f32_e32 v159, v160, v159
	v_mul_f32_e32 v160, 0xbfb8aa3b, v170
	v_max_f32_e32 v44, v44, v169
	s_nop 1
	v_max_f32_dpp v45, v45, v45 quad_perm:[1,0,3,2] row_mask:0xf bank_mask:0xf
	s_nop 1
	v_max_f32_dpp v45, v45, v45 quad_perm:[2,3,0,1] row_mask:0xf bank_mask:0xf
	s_nop 1
	v_max_f32_dpp v45, v45, v45 row_half_mirror row_mask:0xf bank_mask:0xf
	s_nop 1
	v_max_f32_dpp v45, v45, v45 row_ror:8 row_mask:0xf bank_mask:0xf
	v_mov_b32_e32 v169, v45
	s_nop 1
	v_permlane16_swap_b32_e32 v45, v169
	s_nop 0
	v_max_f32_e32 v45, v45, v169
	v_mov_b32_e32 v169, v45
	s_nop 1
	v_permlane32_swap_b32_e32 v45, v169
	s_nop 0
	v_max_f32_e32 v45, v45, v169
	v_mov_b32_e32 v169, v45
	v_exp_f32_e32 v160, v160
	v_add_f32_e32 v154, 1.0, v154
	v_max3_f32 v46, |v152|, 0, |v162|
	v_mul_f32_e32 v166, v174, v166
	v_rcp_f32_e32 v154, v154
	v_add_f32_e32 v156, 1.0, v156
	v_max3_f32 v46, v46, |v163|, |v164|
	v_rcp_f32_e32 v156, v156
	v_add_f32_e32 v158, 1.0, v158
	v_max3_f32 v46, v46, |v165|, |v166|
	v_rcp_f32_e32 v158, v158
	v_add_f32_e32 v160, 1.0, v160
	v_max3_f32 v46, v46, |v167|, |v168|
	s_waitcnt lgkmcnt(0)
	v_max_f32_e32 v169, v169, v169
	v_rcp_f32_e32 v160, v160
	v_max_f32_e32 v45, v45, v169
	s_nop 1
	v_max_f32_dpp v46, v46, v46 quad_perm:[1,0,3,2] row_mask:0xf bank_mask:0xf
	s_nop 1
	v_max_f32_dpp v46, v46, v46 quad_perm:[2,3,0,1] row_mask:0xf bank_mask:0xf
	s_nop 1
	v_max_f32_dpp v46, v46, v46 row_half_mirror row_mask:0xf bank_mask:0xf
	s_nop 1
	v_max_f32_dpp v46, v46, v46 row_ror:8 row_mask:0xf bank_mask:0xf
	v_mov_b32_e32 v169, v46
	s_nop 1
	v_permlane16_swap_b32_e32 v46, v169
	s_nop 0
	v_max_f32_e32 v46, v46, v169
	v_mov_b32_e32 v169, v46
	s_nop 1
	v_permlane32_swap_b32_e32 v46, v169
	s_nop 0
	v_max_f32_e32 v46, v46, v169
	v_mov_b32_e32 v169, v46
	v_mul_f32_e32 v154, v171, v154
	v_mul_f32_e32 v156, v172, v156
	v_max3_f32 v47, |v153|, 0, |v154|
	v_mul_f32_e32 v158, v173, v158
	v_max3_f32 v47, v47, |v155|, |v156|
	v_mul_f32_e32 v160, v170, v160
	v_max3_f32 v47, v47, |v157|, |v158|
	v_max3_f32 v47, v47, |v159|, |v160|
	s_waitcnt lgkmcnt(0)
	v_max_f32_e32 v169, v169, v169
	v_max_f32_e32 v46, v46, v169
	s_nop 1
	v_max_f32_dpp v47, v47, v47 quad_perm:[1,0,3,2] row_mask:0xf bank_mask:0xf
	s_nop 1
	v_max_f32_dpp v47, v47, v47 quad_perm:[2,3,0,1] row_mask:0xf bank_mask:0xf
	s_nop 1
	v_max_f32_dpp v47, v47, v47 row_half_mirror row_mask:0xf bank_mask:0xf
	s_nop 1
	v_max_f32_dpp v47, v47, v47 row_ror:8 row_mask:0xf bank_mask:0xf
	v_mov_b32_e32 v169, v47
	s_nop 1
	v_permlane16_swap_b32_e32 v47, v169
	s_nop 0
	v_max_f32_e32 v47, v47, v169
	v_mov_b32_e32 v169, v47
	s_nop 1
	v_permlane32_swap_b32_e32 v47, v169
	s_nop 0
	v_max_f32_e32 v47, v47, v169
	v_mov_b32_e32 v169, v47
	v_max3_f32 v51, |v48|, 0, |v49|
	v_max3_f32 v51, v51, |v144|, |v146|
	v_max3_f32 v51, v51, |v145|, |v147|
	v_max3_f32 v51, v51, |v148|, |v149|
	s_waitcnt lgkmcnt(0)
	v_max_f32_e32 v169, v169, v169
	v_max_f32_e32 v47, v47, v169
	s_nop 1
	v_max_f32_dpp v51, v51, v51 quad_perm:[1,0,3,2] row_mask:0xf bank_mask:0xf
	s_nop 1
	v_max_f32_dpp v51, v51, v51 quad_perm:[2,3,0,1] row_mask:0xf bank_mask:0xf
	s_nop 1
	v_max_f32_dpp v51, v51, v51 row_half_mirror row_mask:0xf bank_mask:0xf
	s_nop 1
	v_max_f32_dpp v51, v51, v51 row_ror:8 row_mask:0xf bank_mask:0xf
	v_mov_b32_e32 v169, v51
	s_nop 1
	v_permlane16_swap_b32_e32 v51, v169
	s_nop 0
	v_max_f32_e32 v51, v51, v169
	v_mov_b32_e32 v169, v51
	s_nop 1
	v_permlane32_swap_b32_e32 v51, v169
	s_nop 0
	v_max_f32_e32 v51, v51, v169
	v_mov_b32_e32 v169, v51
	s_waitcnt lgkmcnt(0)
	v_max_f32_e32 v169, v169, v169
	v_max_f32_e32 v51, v51, v169
	v_mov_b32_e32 v169, v0
	s_waitcnt lgkmcnt(0)
	v_max_f32_e32 v169, v169, v169
	v_max_f32_e32 v0, v0, v169
	v_mov_b32_e32 v169, v42
	s_waitcnt lgkmcnt(0)
	v_max_f32_e32 v169, v169, v169
	v_max_f32_e32 v42, v42, v169
	v_mov_b32_e32 v169, v43
	s_waitcnt lgkmcnt(0)
	v_max_f32_e32 v169, v169, v169
	v_max_f32_e32 v43, v43, v169
	v_mov_b32_e32 v169, v44
	s_waitcnt lgkmcnt(0)
	v_max_f32_e32 v169, v169, v169
	v_max_f32_e32 v44, v44, v169
	v_mov_b32_e32 v169, v45
	s_waitcnt lgkmcnt(0)
	v_max_f32_e32 v169, v169, v169
	v_max_f32_e32 v45, v45, v169
	v_mov_b32_e32 v169, v46
	s_waitcnt lgkmcnt(0)
	v_max_f32_e32 v169, v169, v169
	v_max_f32_e32 v46, v46, v169
	v_mov_b32_e32 v169, v47
	s_waitcnt lgkmcnt(0)
	v_max_f32_e32 v169, v169, v169
	v_max_f32_e32 v47, v47, v169
	v_mov_b32_e32 v169, v51
	s_waitcnt lgkmcnt(0)
	v_max_f32_e32 v169, v169, v169
	v_max_f32_e32 v51, v51, v169
	v_mov_b32_e32 v169, v0
	s_waitcnt lgkmcnt(0)
	v_max_f32_e32 v169, v169, v169
	v_max_f32_e32 v0, v0, v169
	v_mov_b32_e32 v169, v42
	s_waitcnt lgkmcnt(0)
	v_max_f32_e32 v169, v169, v169
	v_max_f32_e32 v42, v42, v169
	v_mov_b32_e32 v169, v43
	s_waitcnt lgkmcnt(0)
	v_max_f32_e32 v169, v169, v169
	v_max_f32_e32 v43, v43, v169
	v_mov_b32_e32 v169, v44
	s_waitcnt lgkmcnt(0)
	v_max_f32_e32 v169, v169, v169
	v_max_f32_e32 v44, v44, v169
	v_mov_b32_e32 v169, v45
	s_waitcnt lgkmcnt(0)
	v_max_f32_e32 v169, v169, v169
	v_max_f32_e32 v45, v45, v169
	v_mov_b32_e32 v169, v46
	s_waitcnt lgkmcnt(0)
	v_max_f32_e32 v169, v169, v169
	v_max_f32_e32 v46, v46, v169
	v_mov_b32_e32 v169, v47
	s_waitcnt lgkmcnt(0)
	v_max_f32_e32 v169, v169, v169
	v_max_f32_e32 v47, v47, v169
	v_mov_b32_e32 v169, v51
	s_waitcnt lgkmcnt(0)
	v_max_f32_e32 v169, v169, v169
	v_max_f32_e32 v51, v51, v169
	v_mov_b32_e32 v169, v0
	s_waitcnt lgkmcnt(0)
	v_max_f32_e32 v169, v169, v169
	v_max_f32_e32 v0, v0, v169
	v_mov_b32_e32 v169, v42
	s_waitcnt lgkmcnt(0)
	v_max_f32_e32 v169, v169, v169
	v_max_f32_e32 v42, v42, v169
	v_mov_b32_e32 v169, v43
	s_waitcnt lgkmcnt(0)
	v_max_f32_e32 v169, v169, v169
	v_max_f32_e32 v43, v43, v169
	v_mov_b32_e32 v169, v44
	s_waitcnt lgkmcnt(0)
	v_max_f32_e32 v169, v169, v169
	v_max_f32_e32 v44, v44, v169
	v_mov_b32_e32 v169, v45
	s_waitcnt lgkmcnt(0)
	v_max_f32_e32 v169, v169, v169
	v_max_f32_e32 v45, v45, v169
	v_mov_b32_e32 v169, v46
	s_waitcnt lgkmcnt(0)
	v_max_f32_e32 v169, v169, v169
	v_max_f32_e32 v169, v46, v169
	v_mov_b32_e32 v46, v47
	s_waitcnt lgkmcnt(0)
	v_max_f32_e32 v46, v46, v46
	v_max_f32_e32 v47, v47, v46
	v_mov_b32_e32 v46, v51
	s_waitcnt lgkmcnt(0)
	v_max_f32_e32 v46, v46, v46
	v_max_f32_e32 v51, v51, v46
	v_mov_b32_e32 v46, v0
	s_waitcnt lgkmcnt(0)
	v_max_f32_e32 v46, v46, v46
	v_max_f32_e32 v0, v0, v46
	v_mov_b32_e32 v46, v42
	s_waitcnt lgkmcnt(0)
	v_max_f32_e32 v46, v46, v46
	v_max_f32_e32 v46, v42, v46
	v_mov_b32_e32 v42, v43
	s_waitcnt lgkmcnt(0)
	v_max_f32_e32 v42, v42, v42
	v_max_f32_e32 v178, v43, v42
	v_mov_b32_e32 v42, v44
	v_mov_b32_e32 v180, v178
	s_waitcnt lgkmcnt(0)
	v_max_f32_e32 v42, v42, v42
	v_max_f32_e32 v176, v44, v42
	v_mov_b32_e32 v42, v45
	v_mov_b32_e32 v179, v176
	s_waitcnt lgkmcnt(0)
	v_max_f32_e32 v42, v42, v42
	v_max_f32_e32 v175, v45, v42
	v_mov_b32_e32 v42, v169
	v_mov_b32_e32 v177, v175
	s_waitcnt lgkmcnt(0)
	v_max_f32_e32 v42, v42, v42
	v_max_f32_e32 v173, v169, v42
	v_mov_b32_e32 v42, v47
	v_mov_b32_e32 v174, v173
	s_waitcnt lgkmcnt(0)
	v_max_f32_e32 v42, v42, v42
	v_max_f32_e32 v171, v47, v42
	v_mov_b32_e32 v42, v51
	v_mov_b32_e32 v47, v46
	v_mov_b32_e32 v172, v171
	s_waitcnt lgkmcnt(0)
	v_max_f32_e32 v42, v42, v42
	v_max_f32_e32 v169, v51, v42
	v_mov_b32_e32 v42, v0
	v_mov_b32_e32 v170, v169
	v_ashrrev_i32_e32 v51, 31, v50
	v_lshl_add_u64 v[44:45], s[36:37], 0, v[50:51]
	s_waitcnt lgkmcnt(0)
	v_max3_f32 v50, v0, v42, s72
	s_and_saveexec_b64 s[40:41], s[26:27]
	s_cbranch_execz .LBB0_549
	v_lshl_add_u64 v[42:43], v[44:45], 2, s[30:31]
	v_mul_f32_e32 v0, 0x3c010204, v50
	global_store_dword v[42:43], v0, off
